# speedup vs baseline: 1.0040x; 1.0040x over previous
.LBB0_34:
	s_or_b64 exec, exec, s[10:11]
	ds_read_b128 v[18:21], v72
	s_waitcnt vmcnt(3)
	v_cvt_pk_f16_f32 v14, v14, v15
	v_cvt_pk_f16_f32 v15, v16, v17
	v_cvt_pk_f16_f32 v16, v10, v11
	ds_read_b128 v[22:25], v71 offset:41984
	v_cvt_pk_f16_f32 v17, v12, v13
	ds_read_b128 v[10:13], v72 offset:1024
	ds_read_b128 v[26:29], v71 offset:42048
	s_waitcnt vmcnt(1)
	v_cvt_pk_f16_f32 v0, v6, v7
	v_cvt_pk_f16_f32 v1, v8, v9
	v_cvt_pk_f16_f32 v2, v2, v3
	s_waitcnt lgkmcnt(2)
	v_mfma_f32_16x16x32_f16 v[30:33], v[18:21], v[14:17], v[22:25]
	v_cvt_pk_f16_f32 v3, v4, v5
	s_add_i32 s10, s20, s12
	s_nop 0
	v_mfma_f32_16x16x32_f16 v[18:21], v[18:21], v[0:3], v[22:25]
	ds_read_b128 v[4:7], v72 offset:2048
	s_nop 1
	ds_read_b128 v[22:25], v71 offset:42112
	s_waitcnt lgkmcnt(2)
	v_exp_f32_e32 v78, v30
	v_mfma_f32_16x16x32_f16 v[34:37], v[10:13], v[14:17], v[26:29]
	v_exp_f32_e32 v79, v31
	v_exp_f32_e32 v20, v20
	v_mfma_f32_16x16x32_f16 v[8:11], v[10:13], v[0:3], v[26:29]
	ds_read_b128 v[44:47], v71 offset:42176
	s_nop 3
	v_exp_f32_e64 v80, v34 clamp
	v_exp_f32_e64 v81, v35 clamp
	s_waitcnt lgkmcnt(1)
	v_mfma_f32_16x16x32_f16 v[48:51], v[4:7], v[14:17], v[22:25]
	ds_read_b128 v[26:29], v72 offset:3072
	v_exp_f32_e64 v82, v36 clamp
	v_exp_f32_e64 v83, v37 clamp
	v_exp_f32_e32 v21, v21
	v_mfma_f32_16x16x32_f16 v[22:25], v[4:7], v[0:3], v[22:25]
	ds_read_b128 v[52:55], v72 offset:4096
	ds_read_b128 v[56:59], v71 offset:42240
	s_nop 1
	v_exp_f32_e32 v4, v48
	s_waitcnt lgkmcnt(2)
	v_mfma_f32_16x16x32_f16 v[60:63], v[26:29], v[14:17], v[44:47]
	v_exp_f32_e32 v5, v49
	v_exp_f32_e32 v48, v32
	v_exp_f32_e32 v49, v33
	v_mfma_f32_16x16x32_f16 v[26:29], v[26:29], v[0:3], v[44:47]
	ds_read_b128 v[64:67], v71 offset:42304
	v_exp_f32_e32 v6, v50
	v_exp_f32_e32 v7, v51
	s_waitcnt lgkmcnt(1)
	v_mfma_f32_16x16x32_f16 v[74:77], v[52:55], v[14:17], v[56:59]
	ds_read_b128 v[44:47], v72 offset:5120
	v_exp_f32_e32 v50, v18
	v_exp_f32_e32 v51, v19
	v_exp_f32_e32 v26, v26
	v_mfma_f32_16x16x32_f16 v[30:33], v[52:55], v[0:3], v[56:59]
	v_exp_f32_e64 v52, v8 clamp
	v_exp_f32_e64 v53, v9 clamp
	v_exp_f32_e32 v8, v22
	s_waitcnt lgkmcnt(0)
	v_mfma_f32_16x16x32_f16 v[34:37], v[44:47], v[14:17], v[64:67]
	v_exp_f32_e32 v9, v23
	v_exp_f32_e64 v22, v10 clamp
	v_exp_f32_e64 v23, v11 clamp
	v_mfma_f32_16x16x32_f16 v[44:47], v[44:47], v[0:3], v[64:67]
	v_exp_f32_e32 v10, v24
	v_exp_f32_e32 v11, v25
	s_nop 1
	v_exp_f32_e32 v12, v34
	v_exp_f32_e32 v13, v35
	v_exp_f32_e32 v18, v36
	v_exp_f32_e32 v24, v60
	v_exp_f32_e32 v25, v61
	v_exp_f32_e64 v54, v74 clamp
	v_exp_f32_e64 v55, v75 clamp
	v_exp_f32_e32 v34, v62
	v_exp_f32_e32 v35, v63
	v_exp_f32_e64 v56, v76 clamp
	v_exp_f32_e64 v57, v77 clamp
	v_exp_f32_e32 v19, v37
	v_exp_f32_e32 v27, v27
	v_exp_f32_e64 v30, v30 clamp
	v_exp_f32_e64 v31, v31 clamp
	v_exp_f32_e32 v36, v44
	v_exp_f32_e32 v37, v45
	v_exp_f32_e32 v28, v28
	v_exp_f32_e32 v29, v29
	v_exp_f32_e64 v32, v32 clamp
	v_exp_f32_e64 v33, v33 clamp
	v_exp_f32_e32 v44, v46
	v_exp_f32_e32 v45, v47
	v_pk_fma_f32 v[58:59], v[80:81], s[2:3], 1.0 op_sel_hi:[1,0,0]
	v_pk_fma_f32 v[60:61], v[82:83], s[2:3], 1.0 op_sel_hi:[1,0,0]
	v_pk_fma_f32 v[52:53], v[52:53], s[2:3], 1.0 op_sel_hi:[1,0,0]
	v_pk_fma_f32 v[22:23], v[22:23], s[2:3], 1.0 op_sel_hi:[1,0,0]
	v_pk_fma_f32 v[54:55], v[54:55], s[2:3], 1.0 op_sel_hi:[1,0,0]
	v_pk_fma_f32 v[56:57], v[56:57], s[2:3], 1.0 op_sel_hi:[1,0,0]
	v_pk_fma_f32 v[30:31], v[30:31], s[2:3], 1.0 op_sel_hi:[1,0,0]
	v_pk_fma_f32 v[32:33], v[32:33], s[2:3], 1.0 op_sel_hi:[1,0,0]
	v_pk_fma_f32 v[46:47], v[78:79], v[58:59], v[58:59]
	v_pk_fma_f32 v[48:49], v[48:49], v[60:61], v[60:61]
	v_pk_fma_f32 v[50:51], v[50:51], v[52:53], v[52:53]
	v_pk_fma_f32 v[20:21], v[20:21], v[22:23], v[22:23]
	v_pk_fma_f32 v[24:25], v[24:25], v[54:55], v[54:55]
	v_pk_fma_f32 v[34:35], v[34:35], v[56:57], v[56:57]
	v_pk_fma_f32 v[26:27], v[26:27], v[30:31], v[30:31]
	v_pk_fma_f32 v[28:29], v[28:29], v[32:33], v[32:33]
	v_pk_fma_f32 v[58:59], v[58:59], s[6:7], v[40:41] op_sel_hi:[1,0,0] neg_lo:[1,0,0] neg_hi:[1,0,0]
	v_pk_fma_f32 v[60:61], v[60:61], s[6:7], v[40:41] op_sel_hi:[1,0,0] neg_lo:[1,0,0] neg_hi:[1,0,0]
	v_pk_fma_f32 v[52:53], v[52:53], s[6:7], v[40:41] op_sel_hi:[1,0,0] neg_lo:[1,0,0] neg_hi:[1,0,0]
	v_pk_fma_f32 v[22:23], v[22:23], s[6:7], v[40:41] op_sel_hi:[1,0,0] neg_lo:[1,0,0] neg_hi:[1,0,0]
	v_pk_fma_f32 v[54:55], v[54:55], s[6:7], v[40:41] op_sel_hi:[1,0,0] neg_lo:[1,0,0] neg_hi:[1,0,0]
	v_pk_fma_f32 v[56:57], v[56:57], s[6:7], v[40:41] op_sel_hi:[1,0,0] neg_lo:[1,0,0] neg_hi:[1,0,0]
	v_pk_fma_f32 v[30:31], v[30:31], s[6:7], v[40:41] op_sel_hi:[1,0,0] neg_lo:[1,0,0] neg_hi:[1,0,0]
	v_pk_fma_f32 v[32:33], v[32:33], s[6:7], v[40:41] op_sel_hi:[1,0,0] neg_lo:[1,0,0] neg_hi:[1,0,0]
	v_pk_fma_f32 v[46:47], v[4:5], v[46:47], v[46:47]
	v_pk_fma_f32 v[48:49], v[6:7], v[48:49], v[48:49]
	v_pk_fma_f32 v[50:51], v[8:9], v[50:51], v[50:51]
	v_pk_fma_f32 v[20:21], v[10:11], v[20:21], v[20:21]
	v_pk_fma_f32 v[24:25], v[12:13], v[24:25], v[24:25]
	v_pk_fma_f32 v[34:35], v[18:19], v[34:35], v[34:35]
	v_pk_fma_f32 v[26:27], v[36:37], v[26:27], v[26:27]
	v_pk_fma_f32 v[28:29], v[44:45], v[28:29], v[28:29]
	v_rcp_f32_e64 v46, v46 clamp
	v_rcp_f32_e64 v47, v47 clamp
	v_rcp_f32_e64 v48, v48 clamp
	v_rcp_f32_e64 v49, v49 clamp
	v_rcp_f32_e64 v50, v50 clamp
	v_rcp_f32_e64 v51, v51 clamp
	v_rcp_f32_e64 v20, v20 clamp
	v_rcp_f32_e64 v21, v21 clamp
	v_rcp_f32_e64 v24, v24 clamp
	v_rcp_f32_e64 v25, v25 clamp
	v_rcp_f32_e64 v34, v34 clamp
	v_rcp_f32_e64 v35, v35 clamp
	v_rcp_f32_e64 v26, v26 clamp
	v_rcp_f32_e64 v27, v27 clamp
	v_rcp_f32_e64 v28, v28 clamp
	v_rcp_f32_e64 v29, v29 clamp
	v_pk_mul_f32 v[46:47], v[58:59], v[46:47]
	v_pk_mul_f32 v[48:49], v[60:61], v[48:49]
	v_pk_mul_f32 v[50:51], v[52:53], v[50:51]
	v_pk_mul_f32 v[20:21], v[22:23], v[20:21]
	v_pk_mul_f32 v[22:23], v[54:55], v[24:25]
	v_pk_mul_f32 v[24:25], v[56:57], v[34:35]
	v_pk_mul_f32 v[26:27], v[30:31], v[26:27]
	v_pk_mul_f32 v[28:29], v[32:33], v[28:29]
	v_pk_fma_f32 v[4:5], v[4:5], v[46:47], v[46:47]
	v_pk_fma_f32 v[6:7], v[6:7], v[48:49], v[48:49]
	v_pk_fma_f32 v[8:9], v[8:9], v[50:51], v[50:51]
	v_pk_fma_f32 v[10:11], v[10:11], v[20:21], v[20:21]
	v_pk_fma_f32 v[12:13], v[12:13], v[22:23], v[22:23]
	v_pk_fma_f32 v[18:19], v[18:19], v[24:25], v[24:25]
	v_pk_fma_f32 v[30:31], v[36:37], v[26:27], v[26:27]
	v_pk_fma_f32 v[32:33], v[44:45], v[28:29], v[28:29]
	s_nop 0
	v_pk_fma_f32 v[4:5], v[4:5], v[4:5], s[4:5] neg_lo:[1,0,0] neg_hi:[1,0,0] clamp
	v_pk_fma_f32 v[6:7], v[6:7], v[6:7], s[4:5] neg_lo:[1,0,0] neg_hi:[1,0,0] clamp
	v_pk_fma_f32 v[8:9], v[8:9], v[8:9], s[4:5] neg_lo:[1,0,0] neg_hi:[1,0,0] clamp
	v_pk_fma_f32 v[10:11], v[10:11], v[10:11], s[4:5] neg_lo:[1,0,0] neg_hi:[1,0,0] clamp
	v_pk_fma_f32 v[12:13], v[12:13], v[12:13], s[4:5] neg_lo:[1,0,0] neg_hi:[1,0,0] clamp
	v_pk_fma_f32 v[18:19], v[18:19], v[18:19], s[4:5] neg_lo:[1,0,0] neg_hi:[1,0,0] clamp
	v_pk_fma_f32 v[30:31], v[30:31], v[30:31], s[4:5] neg_lo:[1,0,0] neg_hi:[1,0,0] clamp
	s_nop 0
	v_pk_fma_f32 v[32:33], v[32:33], v[32:33], s[4:5] neg_lo:[1,0,0] neg_hi:[1,0,0] clamp
	s_nop 0
	v_pk_fma_f32 v[8:9], v[8:9], v[8:9], s[8:9] op_sel_hi:[1,1,0]
	v_pk_fma_f32 v[10:11], v[10:11], v[10:11], s[8:9] op_sel_hi:[1,1,0]
	v_pk_fma_f32 v[12:13], v[12:13], v[12:13], s[8:9] op_sel_hi:[1,1,0]
	v_pk_fma_f32 v[18:19], v[18:19], v[18:19], s[8:9] op_sel_hi:[1,1,0]
	v_pk_fma_f32 v[32:33], v[32:33], v[32:33], s[8:9] op_sel_hi:[1,1,0]
	v_pk_fma_f32 v[4:5], v[4:5], v[4:5], s[8:9] op_sel_hi:[1,1,0]
	v_pk_fma_f32 v[6:7], v[6:7], v[6:7], s[8:9] op_sel_hi:[1,1,0]
	v_pk_fma_f32 v[30:31], v[30:31], v[30:31], s[8:9] op_sel_hi:[1,1,0]
	v_pk_mul_f32 v[8:9], v[50:51], v[8:9]
	v_pk_mul_f32 v[84:85], v[20:21], v[10:11]
	v_pk_mul_f32 v[86:87], v[22:23], v[12:13]
	v_pk_mul_f32 v[10:11], v[24:25], v[18:19]
	v_pk_mul_f32 v[12:13], v[28:29], v[32:33]
	v_pk_mul_f32 v[64:65], v[46:47], v[4:5]
	v_pk_mul_f32 v[82:83], v[48:49], v[6:7]
	v_pk_mul_f32 v[20:21], v[30:31], v[26:27]
	ds_read_b128 v[4:7], v72 offset:6144
	ds_read_b128 v[22:25], v71 offset:42368
	ds_read_b128 v[26:29], v72 offset:7168
	ds_read_b128 v[30:33], v71 offset:42432
	v_cvt_pk_f16_f32 v19, v84, v85
	v_cvt_pk_f16_f32 v18, v8, v9
	v_cvt_pk_f16_f32 v20, v20, v21
	s_waitcnt lgkmcnt(2)
	v_mfma_f32_16x16x32_f16 v[34:37], v[4:7], v[14:17], v[22:25]
	v_cvt_pk_f16_f32 v21, v12, v13
	v_mfma_f32_16x16x32_f16 v[44:47], v[4:7], v[0:3], v[22:25]
	ds_read_b128 v[4:7], v72 offset:8192
	ds_read_b128 v[48:51], v71 offset:42496
	s_waitcnt lgkmcnt(2)
	v_cvt_pk_f16_f32 v22, v64, v65
	v_mfma_f32_16x16x32_f16 v[52:55], v[26:29], v[14:17], v[30:33]
	v_cvt_pk_f16_f32 v23, v82, v83
	v_cvt_pk_f16_f32 v24, v86, v87
	v_mfma_f32_16x16x32_f16 v[26:29], v[26:29], v[0:3], v[30:33]
	ds_read_b128 v[56:59], v71 offset:42560
	v_exp_f32_e32 v86, v34
	v_exp_f32_e32 v87, v35
	s_waitcnt lgkmcnt(1)
	v_mfma_f32_16x16x32_f16 v[60:63], v[4:7], v[14:17], v[48:51]
	ds_read_b128 v[30:33], v72 offset:9216
	v_exp_f32_e64 v88, v52 clamp
	v_exp_f32_e64 v89, v53 clamp
	v_exp_f32_e64 v90, v54 clamp
	v_mfma_f32_16x16x32_f16 v[48:51], v[4:7], v[0:3], v[48:51]
	ds_read_b128 v[64:67], v72 offset:10240
	ds_read_b128 v[74:77], v71 offset:42624
	s_nop 1
	v_exp_f32_e32 v4, v60
	s_waitcnt lgkmcnt(2)
	v_mfma_f32_16x16x32_f16 v[78:81], v[30:33], v[14:17], v[56:59]
	v_exp_f32_e32 v5, v61
	v_exp_f32_e32 v60, v36
	v_exp_f32_e32 v61, v37
	v_mfma_f32_16x16x32_f16 v[30:33], v[30:33], v[0:3], v[56:59]
	ds_read_b128 v[82:85], v71 offset:42688
	v_exp_f32_e64 v91, v55 clamp
	v_exp_f32_e32 v6, v62
	s_waitcnt lgkmcnt(1)
	v_mfma_f32_16x16x32_f16 v[34:37], v[64:67], v[14:17], v[74:77]
	ds_read_b128 v[56:59], v72 offset:11264
	v_exp_f32_e32 v7, v63
	v_exp_f32_e32 v8, v48
	v_exp_f32_e32 v9, v49
	v_mfma_f32_16x16x32_f16 v[52:55], v[64:67], v[0:3], v[74:77]
	v_exp_f32_e32 v44, v44
	v_exp_f32_e32 v45, v45
	v_exp_f32_e64 v26, v26 clamp
	s_waitcnt lgkmcnt(0)
	v_mfma_f32_16x16x32_f16 v[14:17], v[56:59], v[14:17], v[82:85]
	v_exp_f32_e64 v27, v27 clamp
	v_exp_f32_e32 v46, v46
	v_exp_f32_e32 v47, v47
	v_mfma_f32_16x16x32_f16 v[56:59], v[56:59], v[0:3], v[82:85]
	v_exp_f32_e64 v28, v28 clamp
	s_nop 2
	v_exp_f32_e32 v2, v14
	v_exp_f32_e32 v3, v15
	v_exp_f32_e32 v14, v16
	v_exp_f32_e32 v15, v17
	v_exp_f32_e32 v16, v30
	v_exp_f32_e32 v17, v31
	v_exp_f32_e64 v29, v29 clamp
	v_exp_f32_e32 v0, v50
	v_exp_f32_e32 v1, v51
	v_exp_f32_e32 v48, v78
	v_exp_f32_e32 v49, v79
	v_exp_f32_e64 v34, v34 clamp
	v_exp_f32_e64 v35, v35 clamp
	v_exp_f32_e32 v50, v80
	v_exp_f32_e32 v51, v81
	v_exp_f32_e64 v36, v36 clamp
	v_exp_f32_e64 v37, v37 clamp
	v_exp_f32_e64 v30, v52 clamp
	v_exp_f32_e64 v31, v53 clamp
	v_exp_f32_e32 v52, v56
	v_exp_f32_e32 v53, v57
	v_exp_f32_e32 v32, v32
	v_exp_f32_e32 v33, v33
	v_exp_f32_e64 v54, v54 clamp
	v_exp_f32_e64 v55, v55 clamp
	v_exp_f32_e32 v56, v58
	v_cvt_pk_f16_f32 v25, v10, v11
	v_exp_f32_e32 v57, v59
	v_pk_fma_f32 v[30:31], v[30:31], s[2:3], 1.0 op_sel_hi:[1,0,0]
	v_pk_fma_f32 v[10:11], v[88:89], s[2:3], 1.0 op_sel_hi:[1,0,0]
	v_pk_fma_f32 v[12:13], v[90:91], s[2:3], 1.0 op_sel_hi:[1,0,0]
	v_pk_fma_f32 v[26:27], v[26:27], s[2:3], 1.0 op_sel_hi:[1,0,0]
	v_pk_fma_f32 v[28:29], v[28:29], s[2:3], 1.0 op_sel_hi:[1,0,0]
	v_pk_fma_f32 v[34:35], v[34:35], s[2:3], 1.0 op_sel_hi:[1,0,0]
	v_pk_fma_f32 v[36:37], v[36:37], s[2:3], 1.0 op_sel_hi:[1,0,0]
	v_pk_fma_f32 v[54:55], v[54:55], s[2:3], 1.0 op_sel_hi:[1,0,0]
	v_pk_fma_f32 v[16:17], v[16:17], v[30:31], v[30:31]
	v_pk_fma_f32 v[58:59], v[86:87], v[10:11], v[10:11]
	v_pk_fma_f32 v[10:11], v[10:11], s[6:7], v[40:41] op_sel_hi:[1,0,0] neg_lo:[1,0,0] neg_hi:[1,0,0]
	v_pk_fma_f32 v[60:61], v[60:61], v[12:13], v[12:13]
	v_pk_fma_f32 v[12:13], v[12:13], s[6:7], v[40:41] op_sel_hi:[1,0,0] neg_lo:[1,0,0] neg_hi:[1,0,0]
	v_pk_fma_f32 v[44:45], v[44:45], v[26:27], v[26:27]
	v_pk_fma_f32 v[46:47], v[46:47], v[28:29], v[28:29]
	v_pk_fma_f32 v[48:49], v[48:49], v[34:35], v[34:35]
	v_pk_fma_f32 v[50:51], v[50:51], v[36:37], v[36:37]
	v_pk_fma_f32 v[32:33], v[32:33], v[54:55], v[54:55]
	v_pk_fma_f32 v[16:17], v[52:53], v[16:17], v[16:17]
	v_pk_fma_f32 v[26:27], v[26:27], s[6:7], v[40:41] op_sel_hi:[1,0,0] neg_lo:[1,0,0] neg_hi:[1,0,0]
	v_pk_fma_f32 v[28:29], v[28:29], s[6:7], v[40:41] op_sel_hi:[1,0,0] neg_lo:[1,0,0] neg_hi:[1,0,0]
	v_pk_fma_f32 v[34:35], v[34:35], s[6:7], v[40:41] op_sel_hi:[1,0,0] neg_lo:[1,0,0] neg_hi:[1,0,0]
	v_pk_fma_f32 v[36:37], v[36:37], s[6:7], v[40:41] op_sel_hi:[1,0,0] neg_lo:[1,0,0] neg_hi:[1,0,0]
	v_pk_fma_f32 v[30:31], v[30:31], s[6:7], v[40:41] op_sel_hi:[1,0,0] neg_lo:[1,0,0] neg_hi:[1,0,0]
	v_pk_fma_f32 v[54:55], v[54:55], s[6:7], v[40:41] op_sel_hi:[1,0,0] neg_lo:[1,0,0] neg_hi:[1,0,0]
	v_pk_fma_f32 v[58:59], v[4:5], v[58:59], v[58:59]
	v_pk_fma_f32 v[60:61], v[6:7], v[60:61], v[60:61]
	v_pk_fma_f32 v[44:45], v[8:9], v[44:45], v[44:45]
	v_pk_fma_f32 v[46:47], v[0:1], v[46:47], v[46:47]
	v_pk_fma_f32 v[48:49], v[2:3], v[48:49], v[48:49]
	v_pk_fma_f32 v[50:51], v[14:15], v[50:51], v[50:51]
	v_pk_fma_f32 v[32:33], v[56:57], v[32:33], v[32:33]
	v_rcp_f32_e64 v16, v16 clamp
	v_rcp_f32_e64 v17, v17 clamp
	v_rcp_f32_e64 v58, v58 clamp
	v_rcp_f32_e64 v59, v59 clamp
	v_rcp_f32_e64 v60, v60 clamp
	v_rcp_f32_e64 v61, v61 clamp
	v_rcp_f32_e64 v44, v44 clamp
	v_rcp_f32_e64 v45, v45 clamp
	v_rcp_f32_e64 v46, v46 clamp
	v_rcp_f32_e64 v47, v47 clamp
	v_rcp_f32_e64 v48, v48 clamp
	v_rcp_f32_e64 v49, v49 clamp
	v_rcp_f32_e64 v50, v50 clamp
	v_rcp_f32_e64 v51, v51 clamp
	v_rcp_f32_e64 v32, v32 clamp
	v_rcp_f32_e64 v33, v33 clamp
	v_pk_mul_f32 v[10:11], v[10:11], v[58:59]
	v_pk_mul_f32 v[12:13], v[12:13], v[60:61]
	v_pk_mul_f32 v[26:27], v[26:27], v[44:45]
	v_pk_mul_f32 v[34:35], v[34:35], v[48:49]
	v_pk_mul_f32 v[36:37], v[36:37], v[50:51]
	v_pk_mul_f32 v[28:29], v[28:29], v[46:47]
	v_pk_mul_f32 v[16:17], v[30:31], v[16:17]
	v_pk_mul_f32 v[30:31], v[54:55], v[32:33]
	v_pk_fma_f32 v[4:5], v[4:5], v[10:11], v[10:11]
	v_pk_fma_f32 v[6:7], v[6:7], v[12:13], v[12:13]
	v_pk_fma_f32 v[8:9], v[8:9], v[26:27], v[26:27]
	v_pk_fma_f32 v[2:3], v[2:3], v[34:35], v[34:35]
	v_pk_fma_f32 v[14:15], v[14:15], v[36:37], v[36:37]
	v_pk_fma_f32 v[0:1], v[0:1], v[28:29], v[28:29]
	v_pk_fma_f32 v[32:33], v[52:53], v[16:17], v[16:17]
	v_pk_fma_f32 v[44:45], v[56:57], v[30:31], v[30:31]
	s_nop 0
	v_pk_fma_f32 v[4:5], v[4:5], v[4:5], s[4:5] neg_lo:[1,0,0] neg_hi:[1,0,0] clamp
	v_pk_fma_f32 v[6:7], v[6:7], v[6:7], s[4:5] neg_lo:[1,0,0] neg_hi:[1,0,0] clamp
	v_pk_fma_f32 v[8:9], v[8:9], v[8:9], s[4:5] neg_lo:[1,0,0] neg_hi:[1,0,0] clamp
	v_pk_fma_f32 v[0:1], v[0:1], v[0:1], s[4:5] neg_lo:[1,0,0] neg_hi:[1,0,0] clamp
	v_pk_fma_f32 v[2:3], v[2:3], v[2:3], s[4:5] neg_lo:[1,0,0] neg_hi:[1,0,0] clamp
	v_pk_fma_f32 v[14:15], v[14:15], v[14:15], s[4:5] neg_lo:[1,0,0] neg_hi:[1,0,0] clamp
	v_pk_fma_f32 v[32:33], v[32:33], v[32:33], s[4:5] neg_lo:[1,0,0] neg_hi:[1,0,0] clamp
	s_nop 0
	v_pk_fma_f32 v[44:45], v[44:45], v[44:45], s[4:5] neg_lo:[1,0,0] neg_hi:[1,0,0] clamp
	s_nop 0
	v_pk_fma_f32 v[32:33], v[32:33], v[32:33], s[8:9] op_sel_hi:[1,1,0]
	v_pk_fma_f32 v[4:5], v[4:5], v[4:5], s[8:9] op_sel_hi:[1,1,0]
	v_pk_fma_f32 v[6:7], v[6:7], v[6:7], s[8:9] op_sel_hi:[1,1,0]
	v_pk_fma_f32 v[8:9], v[8:9], v[8:9], s[8:9] op_sel_hi:[1,1,0]
	v_pk_fma_f32 v[0:1], v[0:1], v[0:1], s[8:9] op_sel_hi:[1,1,0]
	v_pk_fma_f32 v[2:3], v[2:3], v[2:3], s[8:9] op_sel_hi:[1,1,0]
	v_pk_fma_f32 v[14:15], v[14:15], v[14:15], s[8:9] op_sel_hi:[1,1,0]
	v_pk_fma_f32 v[44:45], v[44:45], v[44:45], s[8:9] op_sel_hi:[1,1,0]
	v_pk_mul_f32 v[16:17], v[32:33], v[16:17]
	v_pk_mul_f32 v[52:53], v[10:11], v[4:5]
	v_pk_mul_f32 v[54:55], v[12:13], v[6:7]
	v_pk_mul_f32 v[26:27], v[26:27], v[8:9]
	v_pk_mul_f32 v[28:29], v[28:29], v[0:1]
	v_pk_mul_f32 v[56:57], v[34:35], v[2:3]
	v_pk_mul_f32 v[58:59], v[36:37], v[14:15]
	v_pk_mul_f32 v[60:61], v[30:31], v[44:45]
	s_cmp_lt_u32 s33, 8
	s_cbranch_scc1 .Lprio_half
	s_setprio 0
.Lprio_half:
	ds_read_b128 v[0:3], v72 offset:12288
	ds_read_b128 v[4:7], v71 offset:42752
	ds_read_b128 v[8:11], v72 offset:13312
	ds_read_b128 v[12:15], v72 offset:14336
	ds_read_b128 v[34:37], v72 offset:15360
	ds_read_b128 v[44:47], v71 offset:42816
	v_cvt_pk_f16_f32 v30, v52, v53
	v_cvt_pk_f16_f32 v26, v26, v27
	v_cvt_pk_f16_f32 v31, v54, v55
	s_waitcnt lgkmcnt(4)
	v_mfma_f32_16x16x32_f16 v[48:51], v[0:3], v[22:25], v[4:7]
	v_cvt_pk_f16_f32 v32, v56, v57
	v_cvt_pk_f16_f32 v33, v58, v59
	v_cvt_pk_f16_f32 v27, v28, v29
	v_mfma_f32_16x16x32_f16 v[0:3], v[0:3], v[18:21], v[4:7]
	v_cvt_pk_f16_f32 v28, v16, v17
	s_add_i32 s11, s9, s12
	s_waitcnt lgkmcnt(3)
	v_mfma_f32_16x16x32_f16 v[48:51], v[8:11], v[30:33], v[48:51]
	s_cmp_lt_i32 s11, 0x8000
	v_cvt_pk_f16_f32 v29, v60, v61
	s_cselect_b32 s10, s11, s10
	s_ashr_i32 s11, s10, 31
	v_mfma_f32_16x16x32_f16 v[52:55], v[8:11], v[26:29], v[0:3]
	ds_read_b128 v[4:7], v72 offset:17408
	ds_read_b128 v[8:11], v71 offset:42880
	s_lshl_b64 s[10:11], s[10:11], 12
	s_add_u32 s10, s10, s36
	s_addc_u32 s11, s11, s37
	ds_read_b128 v[0:3], v72 offset:16384
	s_waitcnt lgkmcnt(3)
	v_exp_f32_e32 v106, v48
	v_mfma_f32_16x16x32_f16 v[56:59], v[12:15], v[22:25], v[44:47]
	v_exp_f32_e32 v107, v49
	v_exp_f32_e32 v110, v50
	v_mfma_f32_16x16x32_f16 v[12:15], v[12:15], v[18:21], v[44:47]
	v_exp_f32_e32 v111, v51
	v_exp_f32_e32 v114, v52
	v_mfma_f32_16x16x32_f16 v[44:47], v[34:37], v[30:33], v[56:59]
	v_exp_f32_e32 v115, v53
	v_mfma_f32_16x16x32_f16 v[56:59], v[34:37], v[26:29], v[12:15]
	ds_read_b128 v[34:37], v72 offset:19456
	ds_read_b128 v[60:63], v71 offset:42944
	s_nop 4
	v_exp_f32_e64 v108, v44 clamp
	s_waitcnt lgkmcnt(2)
	v_mfma_f32_16x16x32_f16 v[64:67], v[0:3], v[22:25], v[8:11]
	ds_read_b128 v[12:15], v72 offset:18432
	v_exp_f32_e64 v109, v45 clamp
	v_mfma_f32_16x16x32_f16 v[0:3], v[0:3], v[18:21], v[8:11]
	v_exp_f32_e64 v116, v56 clamp
	v_mfma_f32_16x16x32_f16 v[64:67], v[4:7], v[30:33], v[64:67]
	v_exp_f32_e64 v59, v59 clamp
	v_mfma_f32_16x16x32_f16 v[74:77], v[4:7], v[26:29], v[0:3]
	ds_read_b128 v[78:81], v72 offset:20480
	ds_read_b128 v[82:85], v72 offset:21504
	ds_read_b128 v[86:89], v71 offset:43008
	s_waitcnt lgkmcnt(3)
	v_exp_f32_e64 v58, v58 clamp
	v_mfma_f32_16x16x32_f16 v[6:9], v[12:15], v[22:25], v[60:63]
	v_exp_f32_e64 v117, v57 clamp
	v_mfma_f32_16x16x32_f16 v[60:63], v[12:15], v[18:21], v[60:63]
	global_load_dwordx4 v[10:13], v39, s[10:11] offset:16
	global_load_dwordx4 v[14:17], v39, s[10:11]
	global_load_dwordx4 v[2:5], v39, s[10:11] offset:2064
	v_exp_f32_e64 v113, v47 clamp
	v_mfma_f32_16x16x32_f16 v[90:93], v[34:37], v[30:33], v[6:9]
	v_exp_f32_e64 v112, v46 clamp
	v_mfma_f32_16x16x32_f16 v[60:63], v[34:37], v[26:29], v[60:63]
	s_nop 1
	global_load_dwordx4 v[6:9], v39, s[10:11] offset:2048
	ds_read_b128 v[94:97], v72 offset:22528
	ds_read_b128 v[98:101], v72 offset:23552
	ds_read_b128 v[102:105], v71 offset:43072
	s_waitcnt lgkmcnt(3)
	v_exp_f32_e32 v0, v64
	v_mfma_f32_16x16x32_f16 v[44:47], v[78:81], v[22:25], v[86:89]
	v_exp_f32_e32 v1, v65
	v_exp_f32_e32 v34, v66
	v_mfma_f32_16x16x32_f16 v[48:51], v[78:81], v[18:21], v[86:89]
	v_exp_f32_e32 v35, v67
	v_exp_f32_e32 v36, v74
	v_exp_f32_e32 v37, v75
	v_mfma_f32_16x16x32_f16 v[64:67], v[82:85], v[30:33], v[44:47]
	v_exp_f32_e32 v74, v54
	v_exp_f32_e32 v75, v55
	v_exp_f32_e32 v78, v92
	v_mfma_f32_16x16x32_f16 v[50:53], v[82:85], v[26:29], v[48:51]
	v_exp_f32_e32 v44, v76
	v_exp_f32_e32 v45, v77
	v_exp_f32_e32 v76, v90
	s_waitcnt lgkmcnt(0)
	v_mfma_f32_16x16x32_f16 v[46:49], v[94:97], v[22:25], v[102:105]
	v_exp_f32_e32 v77, v91
	v_exp_f32_e64 v64, v64 clamp
	v_exp_f32_e64 v65, v65 clamp
	v_mfma_f32_16x16x32_f16 v[54:57], v[94:97], v[18:21], v[102:105]
	v_exp_f32_e32 v79, v93
	v_exp_f32_e64 v66, v66 clamp
	v_exp_f32_e64 v67, v67 clamp
	v_mfma_f32_16x16x32_f16 v[46:49], v[98:101], v[30:33], v[46:49]
	v_exp_f32_e32 v60, v60
	v_exp_f32_e32 v61, v61
	v_exp_f32_e64 v50, v50 clamp
	v_mfma_f32_16x16x32_f16 v[54:57], v[98:101], v[26:29], v[54:57]
	v_exp_f32_e64 v51, v51 clamp
	s_nop 2
	v_exp_f32_e32 v46, v46
	v_exp_f32_e32 v47, v47
	v_exp_f32_e32 v48, v48
	v_exp_f32_e32 v49, v49
	v_exp_f32_e32 v54, v54
	v_exp_f32_e32 v55, v55
	v_exp_f32_e32 v62, v62
	v_exp_f32_e32 v63, v63
	v_exp_f32_e64 v52, v52 clamp
	v_exp_f32_e64 v53, v53 clamp
	v_exp_f32_e32 v56, v56
	v_exp_f32_e32 v57, v57
	v_pk_fma_f32 v[80:81], v[108:109], s[2:3], 1.0 op_sel_hi:[1,0,0]
	v_pk_fma_f32 v[82:83], v[112:113], s[2:3], 1.0 op_sel_hi:[1,0,0]
	v_pk_fma_f32 v[84:85], v[116:117], s[2:3], 1.0 op_sel_hi:[1,0,0]
	v_pk_fma_f32 v[58:59], v[58:59], s[2:3], 1.0 op_sel_hi:[1,0,0]
	v_pk_fma_f32 v[64:65], v[64:65], s[2:3], 1.0 op_sel_hi:[1,0,0]
	v_pk_fma_f32 v[66:67], v[66:67], s[2:3], 1.0 op_sel_hi:[1,0,0]
	v_pk_fma_f32 v[50:51], v[50:51], s[2:3], 1.0 op_sel_hi:[1,0,0]
	v_pk_fma_f32 v[52:53], v[52:53], s[2:3], 1.0 op_sel_hi:[1,0,0]
	v_pk_fma_f32 v[86:87], v[106:107], v[80:81], v[80:81]
	v_pk_fma_f32 v[88:89], v[110:111], v[82:83], v[82:83]
	v_pk_fma_f32 v[90:91], v[114:115], v[84:85], v[84:85]
	v_pk_fma_f32 v[74:75], v[74:75], v[58:59], v[58:59]
	v_pk_fma_f32 v[76:77], v[76:77], v[64:65], v[64:65]
	v_pk_fma_f32 v[78:79], v[78:79], v[66:67], v[66:67]
	v_pk_fma_f32 v[60:61], v[60:61], v[50:51], v[50:51]
	v_pk_fma_f32 v[62:63], v[62:63], v[52:53], v[52:53]
	v_pk_fma_f32 v[80:81], v[80:81], s[6:7], v[40:41] op_sel_hi:[1,0,0] neg_lo:[1,0,0] neg_hi:[1,0,0]
	v_pk_fma_f32 v[82:83], v[82:83], s[6:7], v[40:41] op_sel_hi:[1,0,0] neg_lo:[1,0,0] neg_hi:[1,0,0]
	v_pk_fma_f32 v[84:85], v[84:85], s[6:7], v[40:41] op_sel_hi:[1,0,0] neg_lo:[1,0,0] neg_hi:[1,0,0]
	v_pk_fma_f32 v[58:59], v[58:59], s[6:7], v[40:41] op_sel_hi:[1,0,0] neg_lo:[1,0,0] neg_hi:[1,0,0]
	v_pk_fma_f32 v[64:65], v[64:65], s[6:7], v[40:41] op_sel_hi:[1,0,0] neg_lo:[1,0,0] neg_hi:[1,0,0]
	v_pk_fma_f32 v[66:67], v[66:67], s[6:7], v[40:41] op_sel_hi:[1,0,0] neg_lo:[1,0,0] neg_hi:[1,0,0]
	v_pk_fma_f32 v[50:51], v[50:51], s[6:7], v[40:41] op_sel_hi:[1,0,0] neg_lo:[1,0,0] neg_hi:[1,0,0]
	v_pk_fma_f32 v[52:53], v[52:53], s[6:7], v[40:41] op_sel_hi:[1,0,0] neg_lo:[1,0,0] neg_hi:[1,0,0]
	v_pk_fma_f32 v[86:87], v[0:1], v[86:87], v[86:87]
	v_pk_fma_f32 v[88:89], v[34:35], v[88:89], v[88:89]
	v_pk_fma_f32 v[90:91], v[36:37], v[90:91], v[90:91]
	v_pk_fma_f32 v[74:75], v[44:45], v[74:75], v[74:75]
	v_pk_fma_f32 v[76:77], v[46:47], v[76:77], v[76:77]
	v_pk_fma_f32 v[78:79], v[48:49], v[78:79], v[78:79]
	v_pk_fma_f32 v[60:61], v[54:55], v[60:61], v[60:61]
	v_pk_fma_f32 v[62:63], v[56:57], v[62:63], v[62:63]
	v_rcp_f32_e64 v86, v86 clamp
	v_rcp_f32_e64 v87, v87 clamp
	v_rcp_f32_e64 v88, v88 clamp
	v_rcp_f32_e64 v89, v89 clamp
	v_rcp_f32_e64 v90, v90 clamp
	v_rcp_f32_e64 v91, v91 clamp
	v_rcp_f32_e64 v74, v74 clamp
	v_rcp_f32_e64 v75, v75 clamp
	v_rcp_f32_e64 v76, v76 clamp
	v_rcp_f32_e64 v77, v77 clamp
	v_rcp_f32_e64 v78, v78 clamp
	v_rcp_f32_e64 v79, v79 clamp
	v_rcp_f32_e64 v60, v60 clamp
	v_rcp_f32_e64 v61, v61 clamp
	v_rcp_f32_e64 v62, v62 clamp
	v_rcp_f32_e64 v63, v63 clamp
	v_pk_mul_f32 v[80:81], v[80:81], v[86:87]
	v_pk_mul_f32 v[82:83], v[82:83], v[88:89]
	v_pk_mul_f32 v[84:85], v[84:85], v[90:91]
	v_pk_mul_f32 v[58:59], v[58:59], v[74:75]
	v_pk_mul_f32 v[64:65], v[64:65], v[76:77]
	v_pk_mul_f32 v[66:67], v[66:67], v[78:79]
	v_pk_mul_f32 v[50:51], v[50:51], v[60:61]
	v_pk_mul_f32 v[60:61], v[52:53], v[62:63]
	v_pk_fma_f32 v[0:1], v[0:1], v[80:81], v[80:81]
	v_pk_fma_f32 v[34:35], v[34:35], v[82:83], v[82:83]
	v_pk_fma_f32 v[36:37], v[36:37], v[84:85], v[84:85]
	v_pk_fma_f32 v[44:45], v[44:45], v[58:59], v[58:59]
	v_pk_fma_f32 v[46:47], v[46:47], v[64:65], v[64:65]
	v_pk_fma_f32 v[48:49], v[48:49], v[66:67], v[66:67]
	v_pk_fma_f32 v[52:53], v[54:55], v[50:51], v[50:51]
	v_pk_fma_f32 v[54:55], v[56:57], v[60:61], v[60:61]
	s_nop 0
	v_pk_fma_f32 v[0:1], v[0:1], v[0:1], s[4:5] neg_lo:[1,0,0] neg_hi:[1,0,0] clamp
	v_pk_fma_f32 v[34:35], v[34:35], v[34:35], s[4:5] neg_lo:[1,0,0] neg_hi:[1,0,0] clamp
	v_pk_fma_f32 v[36:37], v[36:37], v[36:37], s[4:5] neg_lo:[1,0,0] neg_hi:[1,0,0] clamp
	v_pk_fma_f32 v[44:45], v[44:45], v[44:45], s[4:5] neg_lo:[1,0,0] neg_hi:[1,0,0] clamp
	v_pk_fma_f32 v[46:47], v[46:47], v[46:47], s[4:5] neg_lo:[1,0,0] neg_hi:[1,0,0] clamp
	v_pk_fma_f32 v[48:49], v[48:49], v[48:49], s[4:5] neg_lo:[1,0,0] neg_hi:[1,0,0] clamp
	v_pk_fma_f32 v[52:53], v[52:53], v[52:53], s[4:5] neg_lo:[1,0,0] neg_hi:[1,0,0] clamp
	s_nop 0
	v_pk_fma_f32 v[54:55], v[54:55], v[54:55], s[4:5] neg_lo:[1,0,0] neg_hi:[1,0,0] clamp
	s_nop 0
	v_pk_fma_f32 v[0:1], v[0:1], v[0:1], s[8:9] op_sel_hi:[1,1,0]
	v_pk_fma_f32 v[56:57], v[34:35], v[34:35], s[8:9] op_sel_hi:[1,1,0]
	v_pk_fma_f32 v[36:37], v[36:37], v[36:37], s[8:9] op_sel_hi:[1,1,0]
	v_pk_fma_f32 v[44:45], v[44:45], v[44:45], s[8:9] op_sel_hi:[1,1,0]
	v_pk_fma_f32 v[46:47], v[46:47], v[46:47], s[8:9] op_sel_hi:[1,1,0]
	v_pk_fma_f32 v[48:49], v[48:49], v[48:49], s[8:9] op_sel_hi:[1,1,0]
	v_pk_fma_f32 v[62:63], v[52:53], v[52:53], s[8:9] op_sel_hi:[1,1,0]
	v_pk_fma_f32 v[74:75], v[54:55], v[54:55], s[8:9] op_sel_hi:[1,1,0]
	v_pk_mul_f32 v[34:35], v[80:81], v[0:1]
	v_pk_mul_f32 v[56:57], v[82:83], v[56:57]
	v_pk_mul_f32 v[36:37], v[84:85], v[36:37]
	v_pk_mul_f32 v[52:53], v[58:59], v[44:45]
	v_pk_mul_f32 v[54:55], v[64:65], v[46:47]
	v_pk_mul_f32 v[0:1], v[66:67], v[48:49]
	v_pk_mul_f32 v[46:47], v[62:63], v[50:51]
	v_pk_mul_f32 v[44:45], v[60:61], v[74:75]
	ds_read_b128 v[48:51], v72 offset:24576
	ds_read_b128 v[58:61], v71 offset:43136
	ds_read_b128 v[62:65], v72 offset:25600
	ds_read_b128 v[74:77], v72 offset:26624
	ds_read_b128 v[78:81], v72 offset:27648
	ds_read_b128 v[82:85], v71 offset:43200
	v_cvt_pk_f16_f32 v34, v34, v35
	s_waitcnt lgkmcnt(4)
	v_mfma_f32_16x16x32_f16 v[86:89], v[48:51], v[22:25], v[58:61]
	v_cvt_pk_f16_f32 v35, v56, v57
	v_mfma_f32_16x16x32_f16 v[48:51], v[48:51], v[18:21], v[58:61]
	s_waitcnt lgkmcnt(3)
	v_mfma_f32_16x16x32_f16 v[58:61], v[62:65], v[30:33], v[86:89]
	v_mfma_f32_16x16x32_f16 v[86:89], v[62:65], v[26:29], v[48:51]
	ds_read_b128 v[62:65], v72 offset:29696
	ds_read_b128 v[90:93], v71 offset:43264
	s_nop 2
	ds_read_b128 v[48:51], v72 offset:28672
	s_waitcnt lgkmcnt(3)
	v_mfma_f32_16x16x32_f16 v[94:97], v[74:77], v[22:25], v[82:85]
	v_exp_f32_e32 v120, v86
	v_mfma_f32_16x16x32_f16 v[74:77], v[74:77], v[18:21], v[82:85]
	v_exp_f32_e32 v123, v89
	v_mfma_f32_16x16x32_f16 v[82:85], v[78:81], v[30:33], v[94:97]
	v_exp_f32_e32 v122, v88
	v_mfma_f32_16x16x32_f16 v[74:77], v[78:81], v[26:29], v[74:77]
	ds_read_b128 v[78:81], v72 offset:30720
	s_nop 0
	ds_read_b128 v[94:97], v72 offset:31744
	ds_read_b128 v[98:101], v71 offset:43328
	s_waitcnt lgkmcnt(3)
	v_exp_f32_e32 v121, v87
	v_mfma_f32_16x16x32_f16 v[102:105], v[48:51], v[22:25], v[90:93]
	s_nop 0
	v_exp_f32_e64 v66, v82 clamp
	v_exp_f32_e64 v67, v83 clamp
	v_exp_f32_e64 v118, v84 clamp
	v_mfma_f32_16x16x32_f16 v[48:51], v[48:51], v[18:21], v[90:93]
	v_exp_f32_e64 v119, v85 clamp
	v_exp_f32_e64 v124, v74 clamp
	v_exp_f32_e64 v125, v75 clamp
	v_mfma_f32_16x16x32_f16 v[90:93], v[62:65], v[30:33], v[102:105]
	v_exp_f32_e64 v126, v76 clamp
	v_exp_f32_e64 v127, v77 clamp
	v_mfma_f32_16x16x32_f16 v[102:105], v[62:65], v[26:29], v[48:51]
	ds_read_b128 v[106:109], v72 offset:32768
	ds_read_b128 v[110:113], v72 offset:33792
	v_exp_f32_e32 v62, v58
	v_exp_f32_e32 v63, v59
	v_exp_f32_e32 v64, v60
	v_exp_f32_e32 v65, v61
	s_waitcnt lgkmcnt(2)
	v_mfma_f32_16x16x32_f16 v[58:61], v[78:81], v[22:25], v[98:101]
	ds_read_b128 v[114:117], v71 offset:43392
	v_exp_f32_e32 v48, v90
	v_exp_f32_e32 v49, v91
	v_mfma_f32_16x16x32_f16 v[78:81], v[78:81], v[18:21], v[98:101]
	v_exp_f32_e32 v51, v93
	v_mfma_f32_16x16x32_f16 v[82:85], v[94:97], v[30:33], v[58:61]
	v_exp_f32_e32 v50, v92
	v_mfma_f32_16x16x32_f16 v[78:81], v[94:97], v[26:29], v[78:81]
	ds_read_b128 v[86:89], v72 offset:34816
	ds_read_b128 v[90:93], v72 offset:35840
	ds_read_b128 v[94:97], v71 offset:43456
	s_waitcnt lgkmcnt(3)
	v_exp_f32_e32 v58, v102
	v_mfma_f32_16x16x32_f16 v[74:77], v[106:109], v[22:25], v[114:117]
	v_exp_f32_e32 v59, v103
	v_exp_f32_e32 v60, v104
	v_mfma_f32_16x16x32_f16 v[98:101], v[106:109], v[18:21], v[114:117]
	v_exp_f32_e32 v61, v105
	v_exp_f32_e32 v102, v82
	v_exp_f32_e32 v103, v83
	v_exp_f32_e32 v104, v84
	v_mfma_f32_16x16x32_f16 v[74:77], v[110:113], v[30:33], v[74:77]
	v_exp_f32_e32 v105, v85
	v_mfma_f32_16x16x32_f16 v[82:85], v[110:113], v[26:29], v[98:101]
	s_waitcnt lgkmcnt(0)
	v_mfma_f32_16x16x32_f16 v[18:21], v[86:89], v[18:21], v[94:97]
	s_nop 4
	v_exp_f32_e64 v106, v74 clamp
	v_exp_f32_e64 v107, v75 clamp
	v_exp_f32_e64 v108, v76 clamp
	v_exp_f32_e64 v109, v77 clamp
	v_mfma_f32_16x16x32_f16 v[74:77], v[86:89], v[22:25], v[94:97]
	v_cvt_pk_f16_f32 v22, v36, v37
	v_cvt_pk_f16_f32 v23, v52, v53
	v_cvt_pk_f16_f32 v36, v54, v55
	v_mfma_f32_16x16x32_f16 v[18:21], v[90:93], v[26:29], v[18:21]
	v_exp_f32_e32 v52, v78
	v_exp_f32_e32 v53, v79
	v_exp_f32_e64 v54, v82 clamp
	v_mfma_f32_16x16x32_f16 v[30:33], v[90:93], v[30:33], v[74:77]
	v_exp_f32_e64 v55, v83 clamp
	s_nop 2
	v_exp_f32_e32 v18, v18
	v_exp_f32_e32 v19, v19
	v_exp_f32_e32 v26, v80
	v_exp_f32_e32 v27, v81
	v_exp_f32_e32 v30, v30
	v_exp_f32_e32 v31, v31
	v_exp_f32_e32 v32, v32
	v_exp_f32_e32 v33, v33
	v_exp_f32_e64 v28, v84 clamp
	v_exp_f32_e64 v29, v85 clamp
	v_exp_f32_e32 v20, v20
	v_cvt_pk_f16_f32 v24, v46, v47
	v_cvt_pk_f16_f32 v37, v0, v1
	v_cvt_pk_f16_f32 v25, v44, v45
	v_exp_f32_e32 v21, v21
	v_pk_fma_f32 v[0:1], v[66:67], s[2:3], 1.0 op_sel_hi:[1,0,0]
	v_pk_fma_f32 v[44:45], v[118:119], s[2:3], 1.0 op_sel_hi:[1,0,0]
	v_pk_fma_f32 v[46:47], v[124:125], s[2:3], 1.0 op_sel_hi:[1,0,0]
	v_pk_fma_f32 v[56:57], v[126:127], s[2:3], 1.0 op_sel_hi:[1,0,0]
	v_pk_fma_f32 v[66:67], v[106:107], s[2:3], 1.0 op_sel_hi:[1,0,0]
	v_pk_fma_f32 v[74:75], v[108:109], s[2:3], 1.0 op_sel_hi:[1,0,0]
	v_pk_fma_f32 v[54:55], v[54:55], s[2:3], 1.0 op_sel_hi:[1,0,0]
	v_pk_fma_f32 v[28:29], v[28:29], s[2:3], 1.0 op_sel_hi:[1,0,0]
	v_pk_fma_f32 v[62:63], v[62:63], v[0:1], v[0:1]
	v_pk_fma_f32 v[64:65], v[64:65], v[44:45], v[44:45]
	v_pk_fma_f32 v[76:77], v[120:121], v[46:47], v[46:47]
	v_pk_fma_f32 v[78:79], v[122:123], v[56:57], v[56:57]
	v_pk_fma_f32 v[80:81], v[102:103], v[66:67], v[66:67]
	v_pk_fma_f32 v[82:83], v[104:105], v[74:75], v[74:75]
	v_pk_fma_f32 v[52:53], v[52:53], v[54:55], v[54:55]
	v_pk_fma_f32 v[26:27], v[26:27], v[28:29], v[28:29]
	v_pk_fma_f32 v[0:1], v[0:1], s[6:7], v[40:41] op_sel_hi:[1,0,0] neg_lo:[1,0,0] neg_hi:[1,0,0]
	v_pk_fma_f32 v[44:45], v[44:45], s[6:7], v[40:41] op_sel_hi:[1,0,0] neg_lo:[1,0,0] neg_hi:[1,0,0]
	v_pk_fma_f32 v[46:47], v[46:47], s[6:7], v[40:41] op_sel_hi:[1,0,0] neg_lo:[1,0,0] neg_hi:[1,0,0]
	v_pk_fma_f32 v[56:57], v[56:57], s[6:7], v[40:41] op_sel_hi:[1,0,0] neg_lo:[1,0,0] neg_hi:[1,0,0]
	v_pk_fma_f32 v[66:67], v[66:67], s[6:7], v[40:41] op_sel_hi:[1,0,0] neg_lo:[1,0,0] neg_hi:[1,0,0]
	v_pk_fma_f32 v[74:75], v[74:75], s[6:7], v[40:41] op_sel_hi:[1,0,0] neg_lo:[1,0,0] neg_hi:[1,0,0]
	v_pk_fma_f32 v[54:55], v[54:55], s[6:7], v[40:41] op_sel_hi:[1,0,0] neg_lo:[1,0,0] neg_hi:[1,0,0]
	v_pk_fma_f32 v[28:29], v[28:29], s[6:7], v[40:41] op_sel_hi:[1,0,0] neg_lo:[1,0,0] neg_hi:[1,0,0]
	v_pk_fma_f32 v[62:63], v[48:49], v[62:63], v[62:63]
	v_pk_fma_f32 v[64:65], v[50:51], v[64:65], v[64:65]
	v_pk_fma_f32 v[76:77], v[58:59], v[76:77], v[76:77]
	v_pk_fma_f32 v[78:79], v[60:61], v[78:79], v[78:79]
	v_pk_fma_f32 v[80:81], v[30:31], v[80:81], v[80:81]
	v_pk_fma_f32 v[82:83], v[32:33], v[82:83], v[82:83]
	v_pk_fma_f32 v[52:53], v[18:19], v[52:53], v[52:53]
	v_pk_fma_f32 v[26:27], v[20:21], v[26:27], v[26:27]
	v_rcp_f32_e64 v62, v62 clamp
	v_rcp_f32_e64 v63, v63 clamp
	v_rcp_f32_e64 v64, v64 clamp
	v_rcp_f32_e64 v65, v65 clamp
	v_rcp_f32_e64 v76, v76 clamp
	v_rcp_f32_e64 v77, v77 clamp
	v_rcp_f32_e64 v78, v78 clamp
	v_rcp_f32_e64 v79, v79 clamp
	v_rcp_f32_e64 v80, v80 clamp
	v_rcp_f32_e64 v81, v81 clamp
	v_rcp_f32_e64 v82, v82 clamp
	v_rcp_f32_e64 v83, v83 clamp
	v_rcp_f32_e64 v52, v52 clamp
	v_rcp_f32_e64 v53, v53 clamp
	v_rcp_f32_e64 v26, v26 clamp
	v_rcp_f32_e64 v27, v27 clamp
	v_pk_mul_f32 v[52:53], v[54:55], v[52:53]
	v_pk_mul_f32 v[0:1], v[0:1], v[62:63]
	v_pk_mul_f32 v[44:45], v[44:45], v[64:65]
	v_pk_mul_f32 v[46:47], v[46:47], v[76:77]
	v_pk_mul_f32 v[56:57], v[56:57], v[78:79]
	v_pk_mul_f32 v[62:63], v[66:67], v[80:81]
	v_pk_mul_f32 v[64:65], v[74:75], v[82:83]
	v_pk_mul_f32 v[26:27], v[28:29], v[26:27]
	v_pk_fma_f32 v[18:19], v[18:19], v[52:53], v[52:53]
	v_pk_fma_f32 v[28:29], v[48:49], v[0:1], v[0:1]
	v_pk_fma_f32 v[48:49], v[50:51], v[44:45], v[44:45]
	v_pk_fma_f32 v[50:51], v[58:59], v[46:47], v[46:47]
	v_pk_fma_f32 v[54:55], v[60:61], v[56:57], v[56:57]
	v_pk_fma_f32 v[30:31], v[30:31], v[62:63], v[62:63]
	v_pk_fma_f32 v[32:33], v[32:33], v[64:65], v[64:65]
	v_pk_fma_f32 v[20:21], v[20:21], v[26:27], v[26:27]
	s_nop 0
	v_pk_fma_f32 v[28:29], v[28:29], v[28:29], s[4:5] neg_lo:[1,0,0] neg_hi:[1,0,0] clamp
	v_pk_fma_f32 v[48:49], v[48:49], v[48:49], s[4:5] neg_lo:[1,0,0] neg_hi:[1,0,0] clamp
	v_pk_fma_f32 v[50:51], v[50:51], v[50:51], s[4:5] neg_lo:[1,0,0] neg_hi:[1,0,0] clamp
	v_pk_fma_f32 v[54:55], v[54:55], v[54:55], s[4:5] neg_lo:[1,0,0] neg_hi:[1,0,0] clamp
	v_pk_fma_f32 v[30:31], v[30:31], v[30:31], s[4:5] neg_lo:[1,0,0] neg_hi:[1,0,0] clamp
	v_pk_fma_f32 v[32:33], v[32:33], v[32:33], s[4:5] neg_lo:[1,0,0] neg_hi:[1,0,0] clamp
	v_pk_fma_f32 v[18:19], v[18:19], v[18:19], s[4:5] neg_lo:[1,0,0] neg_hi:[1,0,0] clamp
	s_nop 0
	v_pk_fma_f32 v[20:21], v[20:21], v[20:21], s[4:5] neg_lo:[1,0,0] neg_hi:[1,0,0] clamp
	s_nop 0
	v_pk_fma_f32 v[28:29], v[28:29], v[28:29], s[8:9] op_sel_hi:[1,1,0]
	v_pk_fma_f32 v[48:49], v[48:49], v[48:49], s[8:9] op_sel_hi:[1,1,0]
	v_pk_fma_f32 v[50:51], v[50:51], v[50:51], s[8:9] op_sel_hi:[1,1,0]
	v_pk_fma_f32 v[54:55], v[54:55], v[54:55], s[8:9] op_sel_hi:[1,1,0]
	v_pk_fma_f32 v[30:31], v[30:31], v[30:31], s[8:9] op_sel_hi:[1,1,0]
	v_pk_fma_f32 v[32:33], v[32:33], v[32:33], s[8:9] op_sel_hi:[1,1,0]
	v_pk_fma_f32 v[18:19], v[18:19], v[18:19], s[8:9] op_sel_hi:[1,1,0]
	v_pk_fma_f32 v[20:21], v[20:21], v[20:21], s[8:9] op_sel_hi:[1,1,0]
	v_pk_mul_f32 v[0:1], v[0:1], v[28:29]
	v_pk_mul_f32 v[58:59], v[44:45], v[48:49]
	v_pk_mul_f32 v[60:61], v[46:47], v[50:51]
	v_pk_mul_f32 v[54:55], v[56:57], v[54:55]
	v_pk_mul_f32 v[62:63], v[62:63], v[30:31]
	v_pk_mul_f32 v[64:65], v[64:65], v[32:33]
	v_pk_mul_f32 v[66:67], v[18:19], v[52:53]
	v_pk_mul_f32 v[74:75], v[26:27], v[20:21]
	ds_read_b128 v[18:21], v72 offset:36864
	ds_read_b128 v[30:33], v72 offset:37888
	ds_read_b128 v[26:29], v71 offset:43520
	v_cvt_pk_f16_f32 v56, v60, v61
	v_cvt_pk_f16_f32 v57, v54, v55
	v_cvt_pk_f16_f32 v54, v62, v63
	ds_read_b128 v[60:63], v71 offset:43584
	v_cvt_pk_f16_f32 v52, v0, v1
	v_cvt_pk_f16_f32 v53, v58, v59
	s_waitcnt lgkmcnt(1)
	v_mfma_f32_16x16x32_f16 v[48:51], v[18:21], v[34:37], v[26:29]
	v_cvt_pk_f16_f32 v55, v64, v65
	v_cvt_pk_f16_f32 v58, v66, v67
	v_mfma_f32_16x16x32_f16 v[18:21], v[18:21], v[22:25], v[26:29]
	ds_read_b128 v[44:47], v72 offset:40960
	s_add_i32 s12, s12, s3
	s_add_i32 s10, s20, s12
	v_cvt_pk_f16_f32 v59, v74, v75
	v_mfma_f32_16x16x32_f16 v[26:29], v[30:33], v[52:55], v[48:51]
	s_cmp_lt_i32 s10, 0x8000
	v_add_u32_e32 v38, s7, v38
	s_nop 0
	v_mfma_f32_16x16x32_f16 v[18:21], v[30:33], v[56:59], v[18:21]
	ds_read_b128 v[48:51], v72 offset:38912
	ds_read_b128 v[30:33], v72 offset:39936
	s_nop 1
	v_cvt_pk_f16_f32 v1, v28, v29
	v_cvt_pk_f16_f32 v0, v26, v27
	s_waitcnt lgkmcnt(1)
	v_mfma_f32_16x16x32_f16 v[34:37], v[48:51], v[34:37], v[60:63]
	v_pk_max_f16 v27, v1, 0
	v_cvt_pk_f16_f32 v1, v20, v21
	v_pk_max_f16 v26, v0, 0
	v_mfma_f32_16x16x32_f16 v[20:23], v[48:51], v[22:25], v[60:63]
	v_cvt_pk_f16_f32 v0, v18, v19
	v_pk_max_f16 v18, v0, 0
	s_waitcnt lgkmcnt(0)
	v_mfma_f32_16x16x32_f16 v[34:37], v[30:33], v[52:55], v[34:37]
	v_pk_max_f16 v19, v1, 0
	v_mfma_f32_16x16x32_f16 v[20:23], v[30:33], v[56:59], v[20:23]
	s_nop 6
	v_cvt_pk_f16_f32 v0, v34, v35
	v_cvt_pk_f16_f32 v1, v36, v37
	v_pk_max_f16 v28, v0, 0
	v_pk_max_f16 v29, v1, 0
	v_cvt_pk_f16_f32 v0, v20, v21
	v_cvt_pk_f16_f32 v1, v22, v23
	v_pk_max_f16 v20, v0, 0
	v_mfma_f32_16x16x32_f16 v[24:27], v[44:47], v[26:29], 0
	v_pk_max_f16 v21, v1, 0
	s_nop 1
	v_mfma_f32_16x16x32_f16 v[18:21], v[44:47], v[18:21], 0
	s_nop 7
	v_cndmask_b32_e64 v18, v24, v18, s[0:1]
	s_cbranch_scc0 .LBB0_37
